# G1 (SwiGLU) epilogue hidden-tile stores sc1 write-through, to shrink the grid barrier's L2 writeback burst
# baseline (speedup 1.0000x reference)
; __device__ __forceinline__ unsigned cvt_pk_bf16(float lo, float hi) { unsigned r; asm volatile("v_cvt_pk_bf16_f32 %0, %1, %2" : "=v"(r) : "v"(lo), "v"(hi)); return r; }
;     __device__ __forceinline__ void operator()(const f32x4 (&acc)[2][2][4][2], const Unit& u, int wr, int wc, int fr, int fq) const {
;         const int row0 = u.pm * BM + wr * 64 + fr, col0 = CHEAP ? ((u.pn * HALF + wc * 32 + 8 * fq) & 1023) : (u.pn * HALF + wc * 32 + 8 * fq);
; #pragma unroll
;         for (int ai = 0; ai < 2; ++ai)
; #pragma unroll
;             for (int m = 0; m < 4; ++m) { const int row = row0 + ai * HALF + m * 16; bf16_t* rowp = O + (size_t)row * ldc + col0; const float r = tab[u.idx * 256 + (row & 255)];
;                 float o[8];
;                 const float kr = -1.4426950409f * r, r2 = r * r;
; #pragma unroll
;                 for (int n = 0; n < 2; ++n)
; #pragma unroll
;                     for (int e = 0; e < 4; e += 2) { const f32x2 g2 = {acc[ai][0][m][n][e], acc[ai][0][m][n][e + 1]}, u2 = {acc[ai][1][m][n][e], acc[ai][1][m][n][e + 1]};
;                         if (CHEAP) { const f32x2 p = g2 * u2 * r2; o[n * 4 + e] = p[0]; o[n * 4 + e + 1] = p[1]; }
;                         else { const f32x2 x = g2 * kr; const f32x2 d = (f32x2){__builtin_amdgcn_exp2f(x[0]), __builtin_amdgcn_exp2f(x[1])} + 1.0f;
;                             const f32x2 rc = (f32x2){__builtin_amdgcn_rcpf(d[0]), __builtin_amdgcn_rcpf(d[1])} * r2; const f32x2 p = (g2 * u2) * rc; o[n * 4 + e] = p[0]; o[n * 4 + e + 1] = p[1]; } }
;                 u32x4 w; w.x = cvt_pk_bf16(o[0], o[1]); w.y = cvt_pk_bf16(o[2], o[3]); w.z = cvt_pk_bf16(o[4], o[5]); w.w = cvt_pk_bf16(o[6], o[7]);
;                 if (CHEAP == 2) { if (w.x == 0x12345678u && w.y == w.z) *(u32x4*)rowp = w; } else *(u32x4*)rowp = w; }
.LBB0_730:
	s_lshl_b32 s9, s58, 10
	s_add_i32 s9, s9, 0
	s_add_i32 s9, s9, 0x20000
	v_lshl_add_u32 v156, v152, 2, s9
	ds_read_b32 v157, v156
	ds_read_b32 v241, v156 offset:64
	ds_read_b32 v242, v156 offset:128
	ds_read_b32 v243, v156 offset:192
	ds_read_b32 v244, v156 offset:512
	ds_read_b32 v245, v156 offset:576
	ds_read_b32 v246, v156 offset:640
	ds_read_b32 v247, v156 offset:704
	v_pk_mul_f32 v[124:125], v[128:129], v[124:125]
	v_pk_mul_f32 v[126:127], v[130:131], v[126:127]
	v_pk_mul_f32 v[116:117], v[120:121], v[116:117]
	v_lshl_or_b32 v146, s57, 7, v153
	s_waitcnt lgkmcnt(0)
	v_mul_f32_e32 v156, 0xbfb8aa3b, v157
	v_pk_mul_f32 v[160:161], v[128:129], v[156:157] op_sel_hi:[1,0]
	v_pk_mul_f32 v[128:129], v[130:131], v[156:157] op_sel_hi:[1,0]
	v_mul_f32_e32 v158, v157, v157
	v_exp_f32_e32 v128, v128
	v_exp_f32_e32 v129, v129
	v_exp_f32_e32 v160, v160
	v_exp_f32_e32 v161, v161
	v_lshl_add_u32 v155, s44, 8, v150
	v_pk_add_f32 v[128:129], v[128:129], 1.0 op_sel_hi:[1,0]
	v_ashrrev_i32_e32 v147, 31, v146
	v_rcp_f32_e32 v128, v128
	v_rcp_f32_e32 v129, v129
	v_pk_add_f32 v[160:161], v[160:161], 1.0 op_sel_hi:[1,0]
	v_mov_b64_e32 v[144:145], s[4:5]
	v_rcp_f32_e32 v160, v160
	v_pk_mul_f32 v[128:129], v[158:159], v[128:129] op_sel_hi:[0,1]
	v_pk_mul_f32 v[126:127], v[126:127], v[128:129]
	v_pk_mul_f32 v[128:129], v[120:121], v[156:157] op_sel_hi:[1,0]
	v_rcp_f32_e32 v161, v161
	v_exp_f32_e32 v128, v128
	v_exp_f32_e32 v129, v129
	s_movk_i32 s16, 0x1600
	v_pk_mul_f32 v[118:119], v[122:123], v[118:119]
	v_mad_i64_i32 v[148:149], s[36:37], v155, s16, v[144:145]
	v_pk_add_f32 v[128:129], v[128:129], 1.0 op_sel_hi:[1,0]
	v_pk_mul_f32 v[160:161], v[158:159], v[160:161] op_sel_hi:[0,1]
	v_rcp_f32_e32 v128, v128
	v_rcp_f32_e32 v129, v129
	v_pk_mul_f32 v[124:125], v[124:125], v[160:161]
	v_pk_mul_f32 v[108:109], v[112:113], v[108:109]
	v_pk_mul_f32 v[110:111], v[114:115], v[110:111]
	v_pk_mul_f32 v[128:129], v[158:159], v[128:129] op_sel_hi:[0,1]
	v_pk_mul_f32 v[120:121], v[116:117], v[128:129]
	v_pk_mul_f32 v[116:117], v[122:123], v[156:157] op_sel_hi:[1,0]
	v_pk_mul_f32 v[100:101], v[104:105], v[100:101]
	v_exp_f32_e32 v116, v116
	v_exp_f32_e32 v117, v117
	v_pk_mul_f32 v[102:103], v[106:107], v[102:103]
	s_movk_i32 s11, 0xef
	v_pk_mul_f32 v[92:93], v[96:97], v[92:93]
	v_pk_add_f32 v[116:117], v[116:117], 1.0 op_sel_hi:[1,0]
	v_pk_mul_f32 v[94:95], v[98:99], v[94:95]
	v_rcp_f32_e32 v116, v116
	v_rcp_f32_e32 v117, v117
	v_pk_mul_f32 v[84:85], v[88:89], v[84:85]
	v_pk_mul_f32 v[86:87], v[90:91], v[86:87]
	v_pk_mul_f32 v[76:77], v[80:81], v[76:77]
	v_pk_mul_f32 v[116:117], v[158:159], v[116:117] op_sel_hi:[0,1]
	v_pk_mul_f32 v[122:123], v[118:119], v[116:117]
	v_lshlrev_b64 v[116:117], 1, v[146:147]
	v_lshl_add_u64 v[128:129], v[148:149], 0, v[116:117]
	v_cvt_pk_bf16_f32 v118, v124, v125
	v_cvt_pk_bf16_f32 v119, v126, v127
	v_cvt_pk_bf16_f32 v120, v120, v121
	v_cvt_pk_bf16_f32 v121, v122, v123
	global_store_dwordx4 v[128:129], v[118:121], off sc1
	v_pk_mul_f32 v[78:79], v[82:83], v[78:79]
	v_pk_mul_f32 v[68:69], v[72:73], v[68:69]
	v_bitop3_b32 v120, v155, s71, 16 bitop3:0xc8
	v_lshl_add_u32 v120, v120, 2, s9
	v_mov_b32_e32 v121, v241
	v_or_b32_e32 v118, 16, v155
	v_mad_i64_i32 v[118:119], s[36:37], v118, s16, v[144:145]
	v_pk_mul_f32 v[70:71], v[74:75], v[70:71]
	s_waitcnt lgkmcnt(0)
	v_mul_f32_e32 v120, 0xbfb8aa3b, v121
	v_pk_mul_f32 v[124:125], v[112:113], v[120:121] op_sel_hi:[1,0]
	v_pk_mul_f32 v[112:113], v[114:115], v[120:121] op_sel_hi:[1,0]
	v_mul_f32_e32 v122, v121, v121
	v_exp_f32_e32 v112, v112
	v_exp_f32_e32 v113, v113
	v_exp_f32_e32 v124, v124
	v_exp_f32_e32 v125, v125
	v_pk_mul_f32 v[60:61], v[64:65], v[60:61]
	v_pk_add_f32 v[112:113], v[112:113], 1.0 op_sel_hi:[1,0]
	v_pk_mul_f32 v[62:63], v[66:67], v[62:63]
	v_rcp_f32_e32 v112, v112
	v_rcp_f32_e32 v113, v113
	v_pk_add_f32 v[124:125], v[124:125], 1.0 op_sel_hi:[1,0]
	v_pk_mul_f32 v[52:53], v[56:57], v[52:53]
	v_rcp_f32_e32 v124, v124
	v_pk_mul_f32 v[112:113], v[122:123], v[112:113] op_sel_hi:[0,1]
	v_pk_mul_f32 v[110:111], v[110:111], v[112:113]
	v_pk_mul_f32 v[112:113], v[104:105], v[120:121] op_sel_hi:[1,0]
	v_rcp_f32_e32 v125, v125
	v_exp_f32_e32 v112, v112
	v_exp_f32_e32 v113, v113
	v_pk_mul_f32 v[54:55], v[58:59], v[54:55]
	v_pk_mul_f32 v[124:125], v[122:123], v[124:125] op_sel_hi:[0,1]
	v_pk_mul_f32 v[108:109], v[108:109], v[124:125]
	v_pk_add_f32 v[112:113], v[112:113], 1.0 op_sel_hi:[1,0]
	v_pk_mul_f32 v[44:45], v[48:49], v[44:45]
	v_rcp_f32_e32 v112, v112
	v_rcp_f32_e32 v113, v113
	v_pk_mul_f32 v[46:47], v[50:51], v[46:47]
	v_pk_mul_f32 v[36:37], v[40:41], v[36:37]
	v_pk_mul_f32 v[38:39], v[42:43], v[38:39]
	v_pk_mul_f32 v[112:113], v[122:123], v[112:113] op_sel_hi:[0,1]
	v_pk_mul_f32 v[104:105], v[100:101], v[112:113]
	v_pk_mul_f32 v[100:101], v[106:107], v[120:121] op_sel_hi:[1,0]
	v_lshl_add_u64 v[112:113], v[118:119], 0, v[116:117]
	v_exp_f32_e32 v100, v100
	v_exp_f32_e32 v101, v101
	v_pk_mul_f32 v[28:29], v[32:33], v[28:29]
	v_pk_mul_f32 v[30:31], v[34:35], v[30:31]
	v_pk_mul_f32 v[20:21], v[24:25], v[20:21]
	v_pk_add_f32 v[100:101], v[100:101], 1.0 op_sel_hi:[1,0]
	v_pk_mul_f32 v[22:23], v[26:27], v[22:23]
	v_rcp_f32_e32 v100, v100
	v_rcp_f32_e32 v101, v101
	v_pk_mul_f32 v[12:13], v[16:17], v[12:13]
	v_pk_mul_f32 v[14:15], v[18:19], v[14:15]
	v_pk_mul_f32 v[4:5], v[8:9], v[4:5]
	v_pk_mul_f32 v[100:101], v[122:123], v[100:101] op_sel_hi:[0,1]
	v_pk_mul_f32 v[106:107], v[102:103], v[100:101]
	v_cvt_pk_bf16_f32 v100, v108, v109
	v_cvt_pk_bf16_f32 v101, v110, v111
	v_cvt_pk_bf16_f32 v102, v104, v105
	v_pk_mul_f32 v[6:7], v[10:11], v[6:7]
	v_cvt_pk_bf16_f32 v103, v106, v107
	global_store_dwordx4 v[112:113], v[100:103], off sc1
	s_andn2_b64 vcc, exec, s[2:3]
	s_nop 0
	v_bitop3_b32 v102, v155, s11, 32 bitop3:0xc8
	v_lshl_add_u32 v102, v102, 2, s9
	v_mov_b32_e32 v103, v242
	v_or_b32_e32 v100, 32, v155
	v_mad_i64_i32 v[100:101], s[36:37], v100, s16, v[144:145]
	s_waitcnt lgkmcnt(0)
; __device__ __forceinline__ unsigned cvt_pk_bf16(float lo, float hi) { unsigned r; asm volatile("v_cvt_pk_bf16_f32 %0, %1, %2" : "=v"(r) : "v"(lo), "v"(hi)); return r; }
;     __device__ __forceinline__ void operator()(const f32x4 (&acc)[2][2][4][2], const Unit& u, int wr, int wc, int fr, int fq) const {
;     ...
;             for (int m = 0; m < 4; ++m) { const int row = row0 + ai * HALF + m * 16; bf16_t* rowp = O + (size_t)row * ldc + col0; const float r = tab[u.idx * 256 + (row & 255)];
;                 float o[8];
;                 const float kr = -1.4426950409f * r, r2 = r * r;
; #pragma unroll
;                 for (int n = 0; n < 2; ++n)
; #pragma unroll
;                     for (int e = 0; e < 4; e += 2) { const f32x2 g2 = {acc[ai][0][m][n][e], acc[ai][0][m][n][e + 1]}, u2 = {acc[ai][1][m][n][e], acc[ai][1][m][n][e + 1]};
;                         if (CHEAP) { const f32x2 p = g2 * u2 * r2; o[n * 4 + e] = p[0]; o[n * 4 + e + 1] = p[1]; }
;                         else { const f32x2 x = g2 * kr; const f32x2 d = (f32x2){__builtin_amdgcn_exp2f(x[0]), __builtin_amdgcn_exp2f(x[1])} + 1.0f;
;                             const f32x2 rc = (f32x2){__builtin_amdgcn_rcpf(d[0]), __builtin_amdgcn_rcpf(d[1])} * r2; const f32x2 p = (g2 * u2) * rc; o[n * 4 + e] = p[0]; o[n * 4 + e + 1] = p[1]; } }
;                 u32x4 w; w.x = cvt_pk_bf16(o[0], o[1]); w.y = cvt_pk_bf16(o[2], o[3]); w.z = cvt_pk_bf16(o[4], o[5]); w.w = cvt_pk_bf16(o[6], o[7]);
;                 if (CHEAP == 2) { if (w.x == 0x12345678u && w.y == w.z) *(u32x4*)rowp = w; } else *(u32x4*)rowp = w; }
	v_mul_f32_e32 v102, 0xbfb8aa3b, v103
	v_pk_mul_f32 v[106:107], v[96:97], v[102:103] op_sel_hi:[1,0]
	v_pk_mul_f32 v[96:97], v[98:99], v[102:103] op_sel_hi:[1,0]
	v_mul_f32_e32 v104, v103, v103
	v_exp_f32_e32 v96, v96
	v_exp_f32_e32 v97, v97
	v_exp_f32_e32 v106, v106
	v_exp_f32_e32 v107, v107
	v_pk_add_f32 v[96:97], v[96:97], 1.0 op_sel_hi:[1,0]
	s_nop 0
	v_rcp_f32_e32 v96, v96
	v_rcp_f32_e32 v97, v97
	v_pk_add_f32 v[106:107], v[106:107], 1.0 op_sel_hi:[1,0]
	v_pk_mul_f32 v[96:97], v[104:105], v[96:97] op_sel_hi:[0,1]
	v_pk_mul_f32 v[94:95], v[94:95], v[96:97]
	v_pk_mul_f32 v[96:97], v[88:89], v[102:103] op_sel_hi:[1,0]
	v_rcp_f32_e32 v106, v106
	v_exp_f32_e32 v96, v96
	v_exp_f32_e32 v97, v97
	v_rcp_f32_e32 v107, v107
	v_pk_add_f32 v[96:97], v[96:97], 1.0 op_sel_hi:[1,0]
	s_nop 0
	v_rcp_f32_e32 v96, v96
	v_rcp_f32_e32 v97, v97
	v_pk_mul_f32 v[106:107], v[104:105], v[106:107] op_sel_hi:[0,1]
	v_pk_mul_f32 v[92:93], v[92:93], v[106:107]
	v_pk_mul_f32 v[96:97], v[104:105], v[96:97] op_sel_hi:[0,1]
	v_pk_mul_f32 v[88:89], v[84:85], v[96:97]
	v_pk_mul_f32 v[84:85], v[90:91], v[102:103] op_sel_hi:[1,0]
	v_lshl_add_u64 v[96:97], v[100:101], 0, v[116:117]
	v_exp_f32_e32 v84, v84
	v_exp_f32_e32 v85, v85
	s_nop 0
	v_pk_add_f32 v[84:85], v[84:85], 1.0 op_sel_hi:[1,0]
	s_nop 0
	v_rcp_f32_e32 v84, v84
	v_rcp_f32_e32 v85, v85
	s_nop 0
	v_pk_mul_f32 v[84:85], v[104:105], v[84:85] op_sel_hi:[0,1]
	v_pk_mul_f32 v[90:91], v[86:87], v[84:85]
	v_cvt_pk_bf16_f32 v84, v92, v93
	v_cvt_pk_bf16_f32 v85, v94, v95
	v_cvt_pk_bf16_f32 v86, v88, v89
	s_nop 0
	v_cvt_pk_bf16_f32 v87, v90, v91
	global_store_dwordx4 v[96:97], v[84:87], off sc1
	s_nop 1
	v_bitop3_b32 v86, v155, s70, 48 bitop3:0xc8
	v_lshl_add_u32 v86, v86, 2, s9
	v_mov_b32_e32 v87, v243
	v_or_b32_e32 v84, 48, v155
	v_mad_i64_i32 v[84:85], s[36:37], v84, s16, v[144:145]
	s_waitcnt lgkmcnt(0)
	v_mul_f32_e32 v86, 0xbfb8aa3b, v87
	v_pk_mul_f32 v[90:91], v[80:81], v[86:87] op_sel_hi:[1,0]
	v_pk_mul_f32 v[80:81], v[82:83], v[86:87] op_sel_hi:[1,0]
	v_mul_f32_e32 v88, v87, v87
	v_exp_f32_e32 v80, v80
	v_exp_f32_e32 v81, v81
	v_exp_f32_e32 v90, v90
	v_exp_f32_e32 v91, v91
	v_pk_add_f32 v[80:81], v[80:81], 1.0 op_sel_hi:[1,0]
	s_nop 0
	v_rcp_f32_e32 v80, v80
	v_rcp_f32_e32 v81, v81
	v_pk_add_f32 v[90:91], v[90:91], 1.0 op_sel_hi:[1,0]
	v_pk_mul_f32 v[80:81], v[88:89], v[80:81] op_sel_hi:[0,1]
	v_pk_mul_f32 v[78:79], v[78:79], v[80:81]
	v_pk_mul_f32 v[80:81], v[72:73], v[86:87] op_sel_hi:[1,0]
	v_rcp_f32_e32 v90, v90
	v_exp_f32_e32 v80, v80
	v_exp_f32_e32 v81, v81
	v_rcp_f32_e32 v91, v91
	v_pk_add_f32 v[80:81], v[80:81], 1.0 op_sel_hi:[1,0]
	s_nop 0
	v_rcp_f32_e32 v80, v80
	v_rcp_f32_e32 v81, v81
	v_pk_mul_f32 v[90:91], v[88:89], v[90:91] op_sel_hi:[0,1]
	v_pk_mul_f32 v[76:77], v[76:77], v[90:91]
	v_pk_mul_f32 v[80:81], v[88:89], v[80:81] op_sel_hi:[0,1]
	v_pk_mul_f32 v[72:73], v[68:69], v[80:81]
	v_pk_mul_f32 v[68:69], v[74:75], v[86:87] op_sel_hi:[1,0]
	v_lshl_add_u64 v[80:81], v[84:85], 0, v[116:117]
	v_exp_f32_e32 v68, v68
	v_exp_f32_e32 v69, v69
	s_nop 0
	v_pk_add_f32 v[68:69], v[68:69], 1.0 op_sel_hi:[1,0]
	s_nop 0
	v_rcp_f32_e32 v68, v68
	v_rcp_f32_e32 v69, v69
	s_nop 0
	v_pk_mul_f32 v[68:69], v[88:89], v[68:69] op_sel_hi:[0,1]
	v_pk_mul_f32 v[74:75], v[70:71], v[68:69]
	v_cvt_pk_bf16_f32 v68, v76, v77
	v_cvt_pk_bf16_f32 v69, v78, v79
	v_cvt_pk_bf16_f32 v70, v72, v73
	s_nop 0
	v_cvt_pk_bf16_f32 v71, v74, v75
	global_store_dwordx4 v[80:81], v[68:71], off sc1
	s_nop 1
	v_add_u32_e32 v70, 0x80, v155
	v_mad_i64_i32 v[68:69], s[36:37], v70, s16, v[144:145]
	v_and_b32_e32 v70, 0xcf, v70
	v_lshl_add_u32 v70, v70, 2, s9
	v_mov_b32_e32 v71, v244
	s_waitcnt lgkmcnt(0)
	v_mul_f32_e32 v70, 0xbfb8aa3b, v71
	v_pk_mul_f32 v[74:75], v[64:65], v[70:71] op_sel_hi:[1,0]
	v_pk_mul_f32 v[64:65], v[66:67], v[70:71] op_sel_hi:[1,0]
	v_mul_f32_e32 v72, v71, v71
	v_exp_f32_e32 v64, v64
	v_exp_f32_e32 v65, v65
	v_exp_f32_e32 v74, v74
	v_exp_f32_e32 v75, v75
	v_pk_add_f32 v[64:65], v[64:65], 1.0 op_sel_hi:[1,0]
	s_nop 0
	v_rcp_f32_e32 v64, v64
	v_rcp_f32_e32 v65, v65
	v_pk_add_f32 v[74:75], v[74:75], 1.0 op_sel_hi:[1,0]
	v_pk_mul_f32 v[64:65], v[72:73], v[64:65] op_sel_hi:[0,1]
	v_pk_mul_f32 v[62:63], v[62:63], v[64:65]
	v_pk_mul_f32 v[64:65], v[56:57], v[70:71] op_sel_hi:[1,0]
	v_rcp_f32_e32 v74, v74
	v_exp_f32_e32 v64, v64
	v_exp_f32_e32 v65, v65
	v_rcp_f32_e32 v75, v75
	v_pk_add_f32 v[64:65], v[64:65], 1.0 op_sel_hi:[1,0]
	s_nop 0
	v_rcp_f32_e32 v64, v64
	v_rcp_f32_e32 v65, v65
	v_pk_mul_f32 v[74:75], v[72:73], v[74:75] op_sel_hi:[0,1]
	v_pk_mul_f32 v[60:61], v[60:61], v[74:75]
	v_pk_mul_f32 v[64:65], v[72:73], v[64:65] op_sel_hi:[0,1]
	v_pk_mul_f32 v[56:57], v[52:53], v[64:65]
	v_pk_mul_f32 v[52:53], v[58:59], v[70:71] op_sel_hi:[1,0]
	v_lshl_add_u64 v[64:65], v[68:69], 0, v[116:117]
	v_exp_f32_e32 v52, v52
	v_exp_f32_e32 v53, v53
	s_nop 0
	v_pk_add_f32 v[52:53], v[52:53], 1.0 op_sel_hi:[1,0]
	s_nop 0
	v_rcp_f32_e32 v52, v52
	v_rcp_f32_e32 v53, v53
	s_nop 0
	v_pk_mul_f32 v[52:53], v[72:73], v[52:53] op_sel_hi:[0,1]
	v_pk_mul_f32 v[58:59], v[54:55], v[52:53]
	v_cvt_pk_bf16_f32 v52, v60, v61
	v_cvt_pk_bf16_f32 v53, v62, v63
	v_cvt_pk_bf16_f32 v54, v56, v57
	s_nop 0
	v_cvt_pk_bf16_f32 v55, v58, v59
	global_store_dwordx4 v[64:65], v[52:55], off sc1
	s_nop 1
	v_add_u32_e32 v54, 0x90, v155
	v_mad_i64_i32 v[52:53], s[36:37], v54, s16, v[144:145]
	v_and_b32_e32 v54, 0xdf, v54
	v_lshl_add_u32 v54, v54, 2, s9
	v_mov_b32_e32 v55, v245
	s_waitcnt lgkmcnt(0)
; __device__ __forceinline__ unsigned cvt_pk_bf16(float lo, float hi) { unsigned r; asm volatile("v_cvt_pk_bf16_f32 %0, %1, %2" : "=v"(r) : "v"(lo), "v"(hi)); return r; }
;     __device__ __forceinline__ void operator()(const f32x4 (&acc)[2][2][4][2], const Unit& u, int wr, int wc, int fr, int fq) const {
;     ...
;             for (int m = 0; m < 4; ++m) { const int row = row0 + ai * HALF + m * 16; bf16_t* rowp = O + (size_t)row * ldc + col0; const float r = tab[u.idx * 256 + (row & 255)];
;                 float o[8];
;                 const float kr = -1.4426950409f * r, r2 = r * r;
; #pragma unroll
;                 for (int n = 0; n < 2; ++n)
; #pragma unroll
;                     for (int e = 0; e < 4; e += 2) { const f32x2 g2 = {acc[ai][0][m][n][e], acc[ai][0][m][n][e + 1]}, u2 = {acc[ai][1][m][n][e], acc[ai][1][m][n][e + 1]};
;                         if (CHEAP) { const f32x2 p = g2 * u2 * r2; o[n * 4 + e] = p[0]; o[n * 4 + e + 1] = p[1]; }
;                         else { const f32x2 x = g2 * kr; const f32x2 d = (f32x2){__builtin_amdgcn_exp2f(x[0]), __builtin_amdgcn_exp2f(x[1])} + 1.0f;
;                             const f32x2 rc = (f32x2){__builtin_amdgcn_rcpf(d[0]), __builtin_amdgcn_rcpf(d[1])} * r2; const f32x2 p = (g2 * u2) * rc; o[n * 4 + e] = p[0]; o[n * 4 + e + 1] = p[1]; } }
;                 u32x4 w; w.x = cvt_pk_bf16(o[0], o[1]); w.y = cvt_pk_bf16(o[2], o[3]); w.z = cvt_pk_bf16(o[4], o[5]); w.w = cvt_pk_bf16(o[6], o[7]);
;                 if (CHEAP == 2) { if (w.x == 0x12345678u && w.y == w.z) *(u32x4*)rowp = w; } else *(u32x4*)rowp = w; }
	v_mul_f32_e32 v54, 0xbfb8aa3b, v55
	v_pk_mul_f32 v[58:59], v[48:49], v[54:55] op_sel_hi:[1,0]
	v_pk_mul_f32 v[48:49], v[50:51], v[54:55] op_sel_hi:[1,0]
	v_mul_f32_e32 v56, v55, v55
	v_exp_f32_e32 v48, v48
	v_exp_f32_e32 v49, v49
	v_exp_f32_e32 v58, v58
	v_exp_f32_e32 v59, v59
	v_pk_add_f32 v[48:49], v[48:49], 1.0 op_sel_hi:[1,0]
	s_nop 0
	v_rcp_f32_e32 v48, v48
	v_rcp_f32_e32 v49, v49
	v_pk_add_f32 v[58:59], v[58:59], 1.0 op_sel_hi:[1,0]
	v_pk_mul_f32 v[48:49], v[56:57], v[48:49] op_sel_hi:[0,1]
	v_pk_mul_f32 v[46:47], v[46:47], v[48:49]
	v_pk_mul_f32 v[48:49], v[40:41], v[54:55] op_sel_hi:[1,0]
	v_rcp_f32_e32 v58, v58
	v_exp_f32_e32 v48, v48
	v_exp_f32_e32 v49, v49
	v_rcp_f32_e32 v59, v59
	v_pk_add_f32 v[48:49], v[48:49], 1.0 op_sel_hi:[1,0]
	s_nop 0
	v_rcp_f32_e32 v48, v48
	v_rcp_f32_e32 v49, v49
	v_pk_mul_f32 v[58:59], v[56:57], v[58:59] op_sel_hi:[0,1]
	v_pk_mul_f32 v[44:45], v[44:45], v[58:59]
	v_pk_mul_f32 v[48:49], v[56:57], v[48:49] op_sel_hi:[0,1]
	v_pk_mul_f32 v[40:41], v[36:37], v[48:49]
	v_pk_mul_f32 v[36:37], v[42:43], v[54:55] op_sel_hi:[1,0]
	v_lshl_add_u64 v[48:49], v[52:53], 0, v[116:117]
	v_exp_f32_e32 v36, v36
	v_exp_f32_e32 v37, v37
	s_nop 0
	v_pk_add_f32 v[36:37], v[36:37], 1.0 op_sel_hi:[1,0]
	s_nop 0
	v_rcp_f32_e32 v36, v36
	v_rcp_f32_e32 v37, v37
	s_nop 0
	v_pk_mul_f32 v[36:37], v[56:57], v[36:37] op_sel_hi:[0,1]
	v_pk_mul_f32 v[42:43], v[38:39], v[36:37]
	v_cvt_pk_bf16_f32 v36, v44, v45
	v_cvt_pk_bf16_f32 v37, v46, v47
	v_cvt_pk_bf16_f32 v38, v40, v41
	s_nop 0
	v_cvt_pk_bf16_f32 v39, v42, v43
	global_store_dwordx4 v[48:49], v[36:39], off sc1
	s_nop 1
	v_add_u32_e32 v38, 0xa0, v155
	v_mad_i64_i32 v[36:37], s[36:37], v38, s16, v[144:145]
	v_and_b32_e32 v38, 0xef, v38
	v_lshl_add_u32 v38, v38, 2, s9
	v_mov_b32_e32 v39, v246
	s_waitcnt lgkmcnt(0)
	v_mul_f32_e32 v38, 0xbfb8aa3b, v39
	v_pk_mul_f32 v[42:43], v[32:33], v[38:39] op_sel_hi:[1,0]
	v_pk_mul_f32 v[32:33], v[34:35], v[38:39] op_sel_hi:[1,0]
	v_mul_f32_e32 v40, v39, v39
	v_exp_f32_e32 v32, v32
	v_exp_f32_e32 v33, v33
	v_exp_f32_e32 v42, v42
	v_exp_f32_e32 v43, v43
	v_pk_add_f32 v[32:33], v[32:33], 1.0 op_sel_hi:[1,0]
	s_nop 0
	v_rcp_f32_e32 v32, v32
	v_rcp_f32_e32 v33, v33
	v_pk_add_f32 v[42:43], v[42:43], 1.0 op_sel_hi:[1,0]
	v_pk_mul_f32 v[32:33], v[40:41], v[32:33] op_sel_hi:[0,1]
	v_pk_mul_f32 v[30:31], v[30:31], v[32:33]
	v_pk_mul_f32 v[32:33], v[24:25], v[38:39] op_sel_hi:[1,0]
	v_rcp_f32_e32 v42, v42
	v_exp_f32_e32 v32, v32
	v_exp_f32_e32 v33, v33
	v_rcp_f32_e32 v43, v43
	v_pk_add_f32 v[32:33], v[32:33], 1.0 op_sel_hi:[1,0]
	s_nop 0
	v_rcp_f32_e32 v32, v32
	v_rcp_f32_e32 v33, v33
	v_pk_mul_f32 v[42:43], v[40:41], v[42:43] op_sel_hi:[0,1]
	v_pk_mul_f32 v[28:29], v[28:29], v[42:43]
	v_pk_mul_f32 v[32:33], v[40:41], v[32:33] op_sel_hi:[0,1]
	v_pk_mul_f32 v[24:25], v[20:21], v[32:33]
	v_pk_mul_f32 v[20:21], v[26:27], v[38:39] op_sel_hi:[1,0]
	v_lshl_add_u64 v[32:33], v[36:37], 0, v[116:117]
	v_exp_f32_e32 v20, v20
	v_exp_f32_e32 v21, v21
	s_nop 0
	v_pk_add_f32 v[20:21], v[20:21], 1.0 op_sel_hi:[1,0]
	s_nop 0
	v_rcp_f32_e32 v20, v20
	v_rcp_f32_e32 v21, v21
	s_nop 0
	v_pk_mul_f32 v[20:21], v[40:41], v[20:21] op_sel_hi:[0,1]
	v_pk_mul_f32 v[26:27], v[22:23], v[20:21]
	v_cvt_pk_bf16_f32 v20, v28, v29
	v_cvt_pk_bf16_f32 v21, v30, v31
	v_cvt_pk_bf16_f32 v22, v24, v25
	s_nop 0
	v_cvt_pk_bf16_f32 v23, v26, v27
	global_store_dwordx4 v[32:33], v[20:23], off sc1
	s_nop 1
	v_add_u32_e32 v22, 0xb0, v155
	v_mad_i64_i32 v[20:21], s[36:37], v22, s16, v[144:145]
	v_and_b32_e32 v22, 0xff, v22
	v_lshl_add_u32 v22, v22, 2, s9
	v_mov_b32_e32 v23, v247
	s_mov_b64 s[36:37], -1
	s_waitcnt lgkmcnt(0)
	v_mul_f32_e32 v22, 0xbfb8aa3b, v23
	v_pk_mul_f32 v[26:27], v[16:17], v[22:23] op_sel_hi:[1,0]
	v_pk_mul_f32 v[16:17], v[18:19], v[22:23] op_sel_hi:[1,0]
	v_mul_f32_e32 v24, v23, v23
	v_exp_f32_e32 v16, v16
	v_exp_f32_e32 v17, v17
	v_exp_f32_e32 v26, v26
	v_exp_f32_e32 v27, v27
	v_pk_add_f32 v[16:17], v[16:17], 1.0 op_sel_hi:[1,0]
	s_nop 0
	v_rcp_f32_e32 v16, v16
	v_rcp_f32_e32 v17, v17
	v_pk_add_f32 v[26:27], v[26:27], 1.0 op_sel_hi:[1,0]
	v_pk_mul_f32 v[16:17], v[24:25], v[16:17] op_sel_hi:[0,1]
	v_pk_mul_f32 v[14:15], v[14:15], v[16:17]
	v_pk_mul_f32 v[16:17], v[8:9], v[22:23] op_sel_hi:[1,0]
	v_rcp_f32_e32 v26, v26
	v_exp_f32_e32 v16, v16
	v_exp_f32_e32 v17, v17
	v_rcp_f32_e32 v27, v27
	v_pk_add_f32 v[16:17], v[16:17], 1.0 op_sel_hi:[1,0]
	s_nop 0
	v_rcp_f32_e32 v16, v16
	v_rcp_f32_e32 v17, v17
	v_pk_mul_f32 v[26:27], v[24:25], v[26:27] op_sel_hi:[0,1]
	v_pk_mul_f32 v[12:13], v[12:13], v[26:27]
	v_pk_mul_f32 v[16:17], v[24:25], v[16:17] op_sel_hi:[0,1]
	v_pk_mul_f32 v[8:9], v[4:5], v[16:17]
	v_pk_mul_f32 v[4:5], v[10:11], v[22:23] op_sel_hi:[1,0]
	v_lshl_add_u64 v[16:17], v[20:21], 0, v[116:117]
	v_exp_f32_e32 v4, v4
	v_exp_f32_e32 v5, v5
	s_nop 0
	v_pk_add_f32 v[4:5], v[4:5], 1.0 op_sel_hi:[1,0]
	s_nop 0
	v_rcp_f32_e32 v4, v4
	v_rcp_f32_e32 v5, v5
	s_nop 0
	v_pk_mul_f32 v[4:5], v[24:25], v[4:5] op_sel_hi:[0,1]
	v_pk_mul_f32 v[10:11], v[6:7], v[4:5]
	v_cvt_pk_bf16_f32 v4, v12, v13
	v_cvt_pk_bf16_f32 v5, v14, v15
	v_cvt_pk_bf16_f32 v6, v8, v9
	s_nop 0
	v_cvt_pk_bf16_f32 v7, v10, v11
	global_store_dwordx4 v[16:17], v[4:7], off sc1
	s_cbranch_vccnz .LBB0_723
	s_andn2_b64 vcc, exec, s[0:1]
	s_cbranch_vccnz .LBB0_722
	s_barrier
	s_branch .LBB0_722
